# second cached block (block 1 of each wave) kept in the free upper half of the k_final slot area
# speedup vs baseline: 1.0227x; 1.0020x over previous
.LBB2_50:
	s_andn2_b64 vcc, exec, s[16:17]
	s_cbranch_vccnz .LBB2_55
	v_max_f32_e32 v2, v100, v100
	v_max_f32_e32 v2, 0xc6ea6000, v2
	v_and_b32_e32 v4, 0xffff0000, v2
	v_and_b32_e32 v3, 0xffff0000, v99
	v_sub_f32_e32 v5, v2, v4
	v_sub_f32_e32 v3, v99, v3
	v_and_b32_e32 v6, 0xffff0000, v5
	s_mov_b32 s16, 0xffff0000
	v_and_b32_e32 v3, 0xffff0000, v3
	v_sub_f32_e32 v6, v5, v6
	v_lshrrev_b32_e32 v5, 16, v5
	v_or_b32_sdwa v109, v4, v99 dst_sel:DWORD dst_unused:UNUSED_PAD src0_sel:DWORD src1_sel:WORD_1
	v_or_b32_sdwa v108, v3, v99 dst_sel:DWORD dst_unused:UNUSED_PAD src0_sel:DWORD src1_sel:WORD_1
	v_and_or_b32 v110, v6, s16, v5
	v_or_b32_sdwa v111, v2, v4 dst_sel:DWORD dst_unused:UNUSED_PAD src0_sel:WORD_1 src1_sel:DWORD
	s_movk_i32 s16, 0xfc00
	s_nop 0
	v_mfma_f32_32x32x16_bf16 v[2:17], v[40:43], v[108:111], 0
	s_nop 11
	v_cvt_pk_f16_f32 v2, v2, v3
	v_cvt_pk_f16_f32 v3, v4, v5
	v_pk_max_i16 v2, v2, s16 op_sel_hi:[1,0]
	v_pk_max_i16 v3, v3, s16 op_sel_hi:[1,0]
	s_nop 0
	v_exp_f16_e32 v100, v2
	v_exp_f16_e32 v99, v3
	v_exp_f16_sdwa v100, v2 dst_sel:WORD_1 dst_unused:UNUSED_PRESERVE src0_sel:WORD_1
	v_exp_f16_sdwa v99, v3 dst_sel:WORD_1 dst_unused:UNUSED_PRESERVE src0_sel:WORD_1
	v_cvt_pk_f16_f32 v2, v6, v7
	v_cvt_pk_f16_f32 v3, v8, v9
	v_pk_max_i16 v2, v2, s16 op_sel_hi:[1,0]
	v_pk_max_i16 v3, v3, s16 op_sel_hi:[1,0]
	s_nop 0
	v_exp_f16_e32 v102, v2
	v_exp_f16_e32 v101, v3
	v_exp_f16_sdwa v102, v2 dst_sel:WORD_1 dst_unused:UNUSED_PRESERVE src0_sel:WORD_1
	v_exp_f16_sdwa v101, v3 dst_sel:WORD_1 dst_unused:UNUSED_PRESERVE src0_sel:WORD_1
	v_cvt_pk_f16_f32 v2, v10, v11
	v_cvt_pk_f16_f32 v3, v12, v13
	v_pk_max_i16 v2, v2, s16 op_sel_hi:[1,0]
	v_pk_max_i16 v3, v3, s16 op_sel_hi:[1,0]
	s_nop 0
	v_exp_f16_e32 v104, v2
	v_exp_f16_e32 v103, v3
	v_exp_f16_sdwa v104, v2 dst_sel:WORD_1 dst_unused:UNUSED_PRESERVE src0_sel:WORD_1
	v_exp_f16_sdwa v103, v3 dst_sel:WORD_1 dst_unused:UNUSED_PRESERVE src0_sel:WORD_1
	v_cvt_pk_f16_f32 v2, v14, v15
	v_cvt_pk_f16_f32 v3, v16, v17
	v_pk_max_i16 v2, v2, s16 op_sel_hi:[1,0]
	v_pk_max_i16 v3, v3, s16 op_sel_hi:[1,0]
	s_nop 0
	v_exp_f16_e32 v106, v2
	v_exp_f16_e32 v105, v3
	v_exp_f16_sdwa v106, v2 dst_sel:WORD_1 dst_unused:UNUSED_PRESERVE src0_sel:WORD_1
	v_exp_f16_sdwa v105, v3 dst_sel:WORD_1 dst_unused:UNUSED_PRESERVE src0_sel:WORD_1
	v_mfma_f32_32x32x16_bf16 v[2:17], v[36:39], v[108:111], 0
	s_nop 11
	v_cvt_pk_f16_f32 v2, v2, v3
	v_cvt_pk_f16_f32 v3, v4, v5
	v_pk_max_i16 v2, v2, s16 op_sel_hi:[1,0]
	v_pk_max_i16 v3, v3, s16 op_sel_hi:[1,0]
	s_nop 0
	v_exp_f16_e32 v108, v2
	v_exp_f16_e32 v107, v3
	v_exp_f16_sdwa v108, v2 dst_sel:WORD_1 dst_unused:UNUSED_PRESERVE src0_sel:WORD_1
	v_exp_f16_sdwa v107, v3 dst_sel:WORD_1 dst_unused:UNUSED_PRESERVE src0_sel:WORD_1
	v_cvt_pk_f16_f32 v2, v6, v7
	v_cvt_pk_f16_f32 v3, v8, v9
	v_pk_max_i16 v2, v2, s16 op_sel_hi:[1,0]
	v_pk_max_i16 v3, v3, s16 op_sel_hi:[1,0]
	s_nop 0
	v_exp_f16_e32 v110, v2
	v_exp_f16_e32 v109, v3
	v_exp_f16_sdwa v110, v2 dst_sel:WORD_1 dst_unused:UNUSED_PRESERVE src0_sel:WORD_1
	v_exp_f16_sdwa v109, v3 dst_sel:WORD_1 dst_unused:UNUSED_PRESERVE src0_sel:WORD_1
	v_cvt_pk_f16_f32 v2, v10, v11
	v_cvt_pk_f16_f32 v3, v12, v13
	v_pk_max_i16 v2, v2, s16 op_sel_hi:[1,0]
	v_pk_max_i16 v3, v3, s16 op_sel_hi:[1,0]
	s_nop 0
	v_exp_f16_e32 v112, v2
	v_exp_f16_e32 v111, v3
	v_exp_f16_sdwa v112, v2 dst_sel:WORD_1 dst_unused:UNUSED_PRESERVE src0_sel:WORD_1
	v_exp_f16_sdwa v111, v3 dst_sel:WORD_1 dst_unused:UNUSED_PRESERVE src0_sel:WORD_1
	v_cvt_pk_f16_f32 v2, v14, v15
	v_cvt_pk_f16_f32 v3, v16, v17
	v_pk_max_i16 v2, v2, s16 op_sel_hi:[1,0]
	v_pk_max_i16 v3, v3, s16 op_sel_hi:[1,0]
	s_mov_b64 s[16:17], -1
	v_exp_f16_e32 v114, v2
	v_exp_f16_e32 v113, v3
	v_exp_f16_sdwa v114, v2 dst_sel:WORD_1 dst_unused:UNUSED_PRESERVE src0_sel:WORD_1
	v_exp_f16_sdwa v113, v3 dst_sel:WORD_1 dst_unused:UNUSED_PRESERVE src0_sel:WORD_1
	s_cmpk_gt_i32 s60, 0x800
	s_cbranch_scc1 .Lfirst_nocache1
	s_lshl_b32 s66, s46, 16
	s_add_u32 s66, s98, s66
	s_addc_u32 s67, s99, 0
	s_lshl_b32 s68, s27, 12
	s_add_u32 s68, s68, 0x8000
	s_add_u32 s66, s66, s68
	s_addc_u32 s67, s67, 0
	v_lshlrev_b32_e32 v216, 4, v44
	v_mov_b32_e32 v236, v100
	v_mov_b32_e32 v237, v99
	v_mov_b32_e32 v238, v102
	v_mov_b32_e32 v239, v101
	v_mov_b32_e32 v240, v104
	v_mov_b32_e32 v241, v103
	v_mov_b32_e32 v242, v106
	v_mov_b32_e32 v243, v105
	v_mov_b32_e32 v244, v108
	v_mov_b32_e32 v245, v107
	v_mov_b32_e32 v246, v110
	v_mov_b32_e32 v247, v109
	v_mov_b32_e32 v248, v112
	v_mov_b32_e32 v249, v111
	v_mov_b32_e32 v250, v114
	v_mov_b32_e32 v251, v113
	global_store_dwordx4 v216, v[236:239], s[66:67] sc1
	global_store_dwordx4 v216, v[240:243], s[66:67] offset:1024 sc1
	global_store_dwordx4 v216, v[244:247], s[66:67] offset:2048 sc1
	global_store_dwordx4 v216, v[248:251], s[66:67] offset:3072 sc1
.Lfirst_nocache1:
	s_andn2_b64 vcc, exec, s[0:1]
	s_cbranch_vccz .LBB2_56

_Z6k_iterILb0ELb0EEvPKfS1_PKiPK15HIP_vector_typeIfLj4EES7_S1_S1_S3_S1_PfS8_S1_S3_PDF16_PS5_SA_PiSA_SB_:
	s_and_b32 s38, s0, 0xfffff000
	s_mov_b32 s39, s1
	s_load_dwordx2 s[8:9], s[0:1], 0x80
	s_load_dwordx4 s[4:7], s[0:1], 0x70
	s_load_dwordx4 s[16:19], s[0:1], 0x40
	s_load_dwordx2 s[40:41], s[0:1], 0x90
	s_load_dwordx2 s[42:43], s[0:1], 0x88
	v_readfirstlane_b32 s12, v0
	v_cmp_gt_u32_e64 s[14:15], 64, v0
	v_lshlrev_b32_e32 v1, 2, v0
	s_and_saveexec_b64 s[10:11], s[14:15]
	v_mov_b32_e32 v2, 0
	ds_write_b32 v1, v2 offset:5152
	s_or_b64 exec, exec, s[10:11]
	s_lshl_b32 s3, s2, 5
	s_and_b32 s3, s3, 0xe0
	s_lshr_b32 s2, s2, 3
	s_add_i32 s2, s3, s2
	s_lshl_b32 s25, s2, 6
	v_and_b32_e32 v2, 31, v0
	v_or_b32_e32 v4, s25, v2
	v_mov_b32_e32 v5, 0
	s_lshr_b32 s27, s12, 6
	s_lshl_b32 s32, s27, 2
	s_lshr_b32 s32, 0x73261540, s32
	s_lshl_b32 s32, s32, 5
	s_and_b32 s32, s32, 0xe0
	v_or_b32_e32 v176, s32, v2
	v_lshlrev_b32_e32 v177, 4, v176
	v_add_u32_e32 v178, 0x1000, v177
	v_add_u32_e32 v179, 0x2000, v177
	v_add_u32_e32 v180, 0x3000, v177
	v_add_u32_e32 v181, 0x4000, v177
	v_add_u32_e32 v182, 0x5000, v177
	s_mov_b32 s3, 0
	s_lshl_b64 s[34:35], s[2:3], 16
	s_lshl_b32 s33, s2, 2
	s_waitcnt lgkmcnt(0)
	s_load_dword s24, s[8:9], s33 offset:0x0
	s_load_dword s41, s[40:41], s33 offset:0x0
	s_add_u32 s20, s4, s34
	s_addc_u32 s21, s5, s35
	v_lshl_add_u64 v[4:5], v[4:5], 4, s[6:7]
	global_load_dwordx3 v[30:32], v[4:5], off
	global_load_dwordx3 v[26:28], v[4:5], off offset:512
	global_load_dwordx4 v[2:5], v177, s[20:21]
	global_load_dwordx4 v[6:9], v178, s[20:21]
	global_load_dwordx4 v[10:13], v179, s[20:21]
	global_load_dwordx4 v[14:17], v180, s[20:21]
	global_load_dwordx4 v[18:21], v181, s[20:21]
	global_load_dwordx4 v[22:25], v182, s[20:21]
	v_and_b32_e32 v38, 63, v0
	v_mov_b32_e32 v29, 0xff800000
	v_cmp_gt_u32_e64 s[0:1], 32, v38
	s_waitcnt lgkmcnt(0)
	s_cmpk_gt_i32 s24, 0x600
	s_cselect_b64 s[22:23], -1, 0
	s_cmpk_lt_i32 s24, 0x601
	s_cbranch_scc1 .LBB3_6
	s_and_saveexec_b64 s[8:9], s[14:15]
	s_cbranch_execz .LBB3_5
	v_or_b32_e32 v178, s25, v0
	v_mov_b32_e32 v179, 0
	v_lshl_add_u64 v[178:179], v[178:179], 4, s[6:7]
	global_load_dwordx4 v[178:181], v[178:179], off
	v_lshlrev_b32_e32 v177, 4, v0
	s_waitcnt vmcnt(0)
	ds_write_b128 v177, v[178:181] offset:2080

.Lffc_nocache:
	s_cmpk_lt_i32 s41, 0x801
	s_cselect_b32 s36, 1, 0
	s_cbranch_scc0 .Lffc_nocache1
	s_lshl_b32 s46, s27, 12
	s_add_u32 s46, s46, 0x8000
	s_add_u32 s44, s42, s34
	s_addc_u32 s45, s43, s35
	s_add_u32 s44, s44, s46
	s_addc_u32 s45, s45, 0
	v_lshlrev_b32_e32 v183, 4, v38
	global_load_dwordx4 v[200:203], v183, s[44:45]
	global_load_dwordx4 v[204:207], v183, s[44:45] offset:1024
	global_load_dwordx4 v[208:211], v183, s[44:45] offset:2048
	global_load_dwordx4 v[212:215], v183, s[44:45] offset:3072

.LBB3_31:
	s_andn2_b64 vcc, exec, s[4:5]
	s_cbranch_vccnz .LBB3_33
	s_cmp_eq_u32 s36, 0
	s_cbranch_scc1 .Lffc_nb1_compute
	s_waitcnt vmcnt(6)
	v_mov_b32_e32 v98, v200
	v_mov_b32_e32 v97, v201
	v_mov_b32_e32 v100, v202
	v_mov_b32_e32 v99, v203
	v_mov_b32_e32 v102, v204
	v_mov_b32_e32 v101, v205
	v_mov_b32_e32 v104, v206
	v_mov_b32_e32 v103, v207
	v_mov_b32_e32 v106, v208
	v_mov_b32_e32 v105, v209
	v_mov_b32_e32 v108, v210
	v_mov_b32_e32 v107, v211
	v_mov_b32_e32 v110, v212
	v_mov_b32_e32 v109, v213
	v_mov_b32_e32 v112, v214
	v_mov_b32_e32 v111, v215
	s_mov_b64 s[4:5], -1
	s_andn2_b64 vcc, exec, s[2:3]
	s_cbranch_vccz .LBB3_34
	s_branch .LBB3_37
.Lffc_nb1_compute:
	v_max_f32_e32 v2, v98, v98
	v_max_f32_e32 v2, 0xc6ea6000, v2
	v_and_b32_e32 v4, 0xffff0000, v2
	v_and_b32_e32 v3, 0xffff0000, v97
	v_sub_f32_e32 v5, v2, v4
	v_sub_f32_e32 v3, v97, v3
	v_and_b32_e32 v6, 0xffff0000, v5
	s_mov_b32 s4, 0xffff0000
	v_and_b32_e32 v3, 0xffff0000, v3
	v_sub_f32_e32 v6, v5, v6
	v_lshrrev_b32_e32 v5, 16, v5
	v_or_b32_sdwa v107, v4, v97 dst_sel:DWORD dst_unused:UNUSED_PAD src0_sel:DWORD src1_sel:WORD_1
	v_or_b32_sdwa v106, v3, v97 dst_sel:DWORD dst_unused:UNUSED_PAD src0_sel:DWORD src1_sel:WORD_1
	v_and_or_b32 v108, v6, s4, v5
	v_or_b32_sdwa v109, v2, v4 dst_sel:DWORD dst_unused:UNUSED_PAD src0_sel:WORD_1 src1_sel:DWORD
	s_movk_i32 s4, 0xfc00
	s_nop 0
	v_mfma_f32_32x32x16_bf16 v[2:17], v[22:25], v[106:109], 0
	s_nop 11
	v_cvt_pk_f16_f32 v2, v2, v3
	v_cvt_pk_f16_f32 v3, v4, v5
	v_pk_max_i16 v2, v2, s4 op_sel_hi:[1,0]
	v_pk_max_i16 v3, v3, s4 op_sel_hi:[1,0]
	s_nop 0
	v_exp_f16_e32 v98, v2
	v_exp_f16_e32 v97, v3
	v_exp_f16_sdwa v98, v2 dst_sel:WORD_1 dst_unused:UNUSED_PRESERVE src0_sel:WORD_1
	v_exp_f16_sdwa v97, v3 dst_sel:WORD_1 dst_unused:UNUSED_PRESERVE src0_sel:WORD_1
	v_cvt_pk_f16_f32 v2, v6, v7
	v_cvt_pk_f16_f32 v3, v8, v9
	v_pk_max_i16 v2, v2, s4 op_sel_hi:[1,0]
	v_pk_max_i16 v3, v3, s4 op_sel_hi:[1,0]
	s_nop 0
	v_exp_f16_e32 v100, v2
	v_exp_f16_e32 v99, v3
	v_exp_f16_sdwa v100, v2 dst_sel:WORD_1 dst_unused:UNUSED_PRESERVE src0_sel:WORD_1
	v_exp_f16_sdwa v99, v3 dst_sel:WORD_1 dst_unused:UNUSED_PRESERVE src0_sel:WORD_1
	v_cvt_pk_f16_f32 v2, v10, v11
	v_cvt_pk_f16_f32 v3, v12, v13
	v_pk_max_i16 v2, v2, s4 op_sel_hi:[1,0]
	v_pk_max_i16 v3, v3, s4 op_sel_hi:[1,0]
	s_nop 0
	v_exp_f16_e32 v102, v2
	v_exp_f16_e32 v101, v3
	v_exp_f16_sdwa v102, v2 dst_sel:WORD_1 dst_unused:UNUSED_PRESERVE src0_sel:WORD_1
	v_exp_f16_sdwa v101, v3 dst_sel:WORD_1 dst_unused:UNUSED_PRESERVE src0_sel:WORD_1
	v_cvt_pk_f16_f32 v2, v14, v15
	v_cvt_pk_f16_f32 v3, v16, v17
	v_pk_max_i16 v2, v2, s4 op_sel_hi:[1,0]
	v_pk_max_i16 v3, v3, s4 op_sel_hi:[1,0]
	s_nop 0
	v_exp_f16_e32 v104, v2
	v_exp_f16_e32 v103, v3
	v_exp_f16_sdwa v104, v2 dst_sel:WORD_1 dst_unused:UNUSED_PRESERVE src0_sel:WORD_1
	v_exp_f16_sdwa v103, v3 dst_sel:WORD_1 dst_unused:UNUSED_PRESERVE src0_sel:WORD_1
	v_mfma_f32_32x32x16_bf16 v[2:17], v[18:21], v[106:109], 0
	s_nop 11
	v_cvt_pk_f16_f32 v2, v2, v3
	v_cvt_pk_f16_f32 v3, v4, v5
	v_pk_max_i16 v2, v2, s4 op_sel_hi:[1,0]
	v_pk_max_i16 v3, v3, s4 op_sel_hi:[1,0]
	s_nop 0
	v_exp_f16_e32 v106, v2
	v_exp_f16_e32 v105, v3
	v_exp_f16_sdwa v106, v2 dst_sel:WORD_1 dst_unused:UNUSED_PRESERVE src0_sel:WORD_1
	v_exp_f16_sdwa v105, v3 dst_sel:WORD_1 dst_unused:UNUSED_PRESERVE src0_sel:WORD_1
	v_cvt_pk_f16_f32 v2, v6, v7
	v_cvt_pk_f16_f32 v3, v8, v9
	v_pk_max_i16 v2, v2, s4 op_sel_hi:[1,0]
	v_pk_max_i16 v3, v3, s4 op_sel_hi:[1,0]
	s_nop 0
	v_exp_f16_e32 v108, v2
	v_exp_f16_e32 v107, v3
	v_exp_f16_sdwa v108, v2 dst_sel:WORD_1 dst_unused:UNUSED_PRESERVE src0_sel:WORD_1
	v_exp_f16_sdwa v107, v3 dst_sel:WORD_1 dst_unused:UNUSED_PRESERVE src0_sel:WORD_1
	v_cvt_pk_f16_f32 v2, v10, v11
	v_cvt_pk_f16_f32 v3, v12, v13
	v_pk_max_i16 v2, v2, s4 op_sel_hi:[1,0]
	v_pk_max_i16 v3, v3, s4 op_sel_hi:[1,0]
	s_nop 0
	v_exp_f16_e32 v110, v2
	v_exp_f16_e32 v109, v3
	v_exp_f16_sdwa v110, v2 dst_sel:WORD_1 dst_unused:UNUSED_PRESERVE src0_sel:WORD_1
	v_exp_f16_sdwa v109, v3 dst_sel:WORD_1 dst_unused:UNUSED_PRESERVE src0_sel:WORD_1
	v_cvt_pk_f16_f32 v2, v14, v15
	v_cvt_pk_f16_f32 v3, v16, v17
	v_pk_max_i16 v2, v2, s4 op_sel_hi:[1,0]
	v_pk_max_i16 v3, v3, s4 op_sel_hi:[1,0]
	s_mov_b64 s[4:5], -1
	v_exp_f16_e32 v112, v2
	v_exp_f16_e32 v111, v3
	v_exp_f16_sdwa v112, v2 dst_sel:WORD_1 dst_unused:UNUSED_PRESERVE src0_sel:WORD_1
	v_exp_f16_sdwa v111, v3 dst_sel:WORD_1 dst_unused:UNUSED_PRESERVE src0_sel:WORD_1
	s_andn2_b64 vcc, exec, s[2:3]
	s_cbranch_vccz .LBB3_34
	s_branch .LBB3_37

	.amdhsa_kernel _Z6k_iterILb0ELb0EEvPKfS1_PKiPK15HIP_vector_typeIfLj4EES7_S1_S1_S3_S1_PfS8_S1_S3_PDF16_PS5_SA_PiSA_SB_
		.amdhsa_group_segment_fixed_size 5808
		.amdhsa_private_segment_fixed_size 0
		.amdhsa_kernarg_size 152
		.amdhsa_user_sgpr_count 2
		.amdhsa_user_sgpr_dispatch_ptr 0
		.amdhsa_user_sgpr_queue_ptr 0
		.amdhsa_user_sgpr_kernarg_segment_ptr 1
		.amdhsa_user_sgpr_dispatch_id 0
		.amdhsa_user_sgpr_kernarg_preload_length 0
		.amdhsa_user_sgpr_kernarg_preload_offset 0
		.amdhsa_user_sgpr_private_segment_size 0
		.amdhsa_uses_dynamic_stack 0
		.amdhsa_enable_private_segment 0
		.amdhsa_system_sgpr_workgroup_id_x 1
		.amdhsa_system_sgpr_workgroup_id_y 0
		.amdhsa_system_sgpr_workgroup_id_z 0
		.amdhsa_system_sgpr_workgroup_info 0
		.amdhsa_system_vgpr_workitem_id 0
		.amdhsa_next_free_vgpr 216
		.amdhsa_next_free_sgpr 48
		.amdhsa_accum_offset 216
		.amdhsa_reserve_vcc 1
		.amdhsa_float_round_mode_32 0
		.amdhsa_float_round_mode_16_64 0
		.amdhsa_float_denorm_mode_32 3
		.amdhsa_float_denorm_mode_16_64 3
		.amdhsa_dx10_clamp 1
		.amdhsa_ieee_mode 1
		.amdhsa_fp16_overflow 0
		.amdhsa_tg_split 0
		.amdhsa_exception_fp_ieee_invalid_op 0
		.amdhsa_exception_fp_denorm_src 0
		.amdhsa_exception_fp_ieee_div_zero 0
		.amdhsa_exception_fp_ieee_overflow 0
		.amdhsa_exception_fp_ieee_underflow 0
		.amdhsa_exception_fp_ieee_inexact 0
		.amdhsa_exception_int_div_zero 0
	.end_amdhsa_kernel

_Z6k_iterILb0ELb1EEvPKfS1_PKiPK15HIP_vector_typeIfLj4EES7_S1_S1_S3_S1_PfS8_S1_S3_PDF16_PS5_SA_PiSA_SB_:
	s_and_b32 s38, s0, 0xfffff000
	s_mov_b32 s39, s1
	s_load_dwordx2 s[8:9], s[0:1], 0x80
	s_load_dwordx4 s[4:7], s[0:1], 0x70
	s_load_dwordx4 s[16:19], s[0:1], 0x40
	s_load_dwordx2 s[40:41], s[0:1], 0x90
	s_load_dwordx2 s[22:23], s[0:1], 0x50
	s_load_dwordx2 s[42:43], s[0:1], 0x88
	v_readfirstlane_b32 s12, v0
	v_cmp_gt_u32_e64 s[14:15], 64, v0
	v_lshlrev_b32_e32 v1, 2, v0
	s_and_saveexec_b64 s[10:11], s[14:15]
	v_mov_b32_e32 v2, 0
	ds_write_b32 v1, v2 offset:5152
	s_or_b64 exec, exec, s[10:11]
	s_lshl_b32 s3, s2, 5
	s_and_b32 s3, s3, 0xe0
	s_lshr_b32 s2, s2, 3
	s_add_i32 s2, s3, s2
	s_lshl_b32 s29, s2, 6
	v_and_b32_e32 v2, 31, v0
	v_or_b32_e32 v4, s29, v2
	v_mov_b32_e32 v5, 0
	s_lshr_b32 s30, s12, 6
	s_lshl_b32 s32, s30, 2
	s_lshr_b32 s32, 0x73261540, s32
	s_lshl_b32 s32, s32, 5
	s_and_b32 s32, s32, 0xe0
	v_or_b32_e32 v176, s32, v2
	v_lshlrev_b32_e32 v177, 4, v176
	v_add_u32_e32 v178, 0x1000, v177
	v_add_u32_e32 v179, 0x2000, v177
	v_add_u32_e32 v180, 0x3000, v177
	v_add_u32_e32 v181, 0x4000, v177
	v_add_u32_e32 v182, 0x5000, v177
	s_mov_b32 s3, 0
	s_lshl_b64 s[34:35], s[2:3], 16
	s_lshl_b32 s33, s2, 2
	s_waitcnt lgkmcnt(0)
	s_load_dword s26, s[8:9], s33 offset:0x0
	s_load_dword s41, s[40:41], s33 offset:0x0
	s_add_u32 s20, s4, s34
	s_addc_u32 s21, s5, s35
	v_lshl_add_u64 v[4:5], v[4:5], 4, s[6:7]
	global_load_dwordx3 v[30:32], v[4:5], off
	global_load_dwordx3 v[26:28], v[4:5], off offset:512
	global_load_dwordx4 v[2:5], v177, s[20:21]
	global_load_dwordx4 v[6:9], v178, s[20:21]
	global_load_dwordx4 v[10:13], v179, s[20:21]
	global_load_dwordx4 v[14:17], v180, s[20:21]
	global_load_dwordx4 v[18:21], v181, s[20:21]
	global_load_dwordx4 v[22:25], v182, s[20:21]
	v_and_b32_e32 v38, 63, v0
	v_mov_b32_e32 v29, 0xff800000
	v_cmp_gt_u32_e64 s[0:1], 32, v38
	s_waitcnt lgkmcnt(0)
	s_cmpk_gt_i32 s26, 0x600
	s_cselect_b64 s[24:25], -1, 0
	s_cmpk_lt_i32 s26, 0x601
	s_cbranch_scc1 .LBB4_6
	s_and_saveexec_b64 s[8:9], s[14:15]
	s_cbranch_execz .LBB4_5
	v_or_b32_e32 v178, s29, v0
	v_mov_b32_e32 v179, 0
	v_lshl_add_u64 v[178:179], v[178:179], 4, s[6:7]
	global_load_dwordx4 v[178:181], v[178:179], off
	v_lshlrev_b32_e32 v177, 4, v0
	s_waitcnt vmcnt(0)
	ds_write_b128 v177, v[178:181] offset:2080

.Lftc_nocache:
	s_cmpk_lt_i32 s41, 0x801
	s_cselect_b32 s36, 1, 0
	s_cbranch_scc0 .Lftc_nocache1
	s_lshl_b32 s46, s30, 12
	s_add_u32 s46, s46, 0x8000
	s_add_u32 s44, s42, s34
	s_addc_u32 s45, s43, s35
	s_add_u32 s44, s44, s46
	s_addc_u32 s45, s45, 0
	v_lshlrev_b32_e32 v183, 4, v38
	global_load_dwordx4 v[200:203], v183, s[44:45]
	global_load_dwordx4 v[204:207], v183, s[44:45] offset:1024
	global_load_dwordx4 v[208:211], v183, s[44:45] offset:2048
	global_load_dwordx4 v[212:215], v183, s[44:45] offset:3072

.LBB4_39:
	s_waitcnt vmcnt(5)
	v_rcp_f32_e32 v2, v133
	s_waitcnt vmcnt(4)
	v_rcp_f32_e32 v3, v132
	s_waitcnt vmcnt(3)
	v_rcp_f32_e32 v4, v131
	v_cmp_lt_f32_e32 vcc, 0, v133
	s_waitcnt vmcnt(2)
	v_rcp_f32_e32 v5, v130
	s_waitcnt vmcnt(1)
	v_rcp_f32_e32 v6, v129
	v_cndmask_b32_e32 v2, 0, v2, vcc
	v_cmp_lt_f32_e32 vcc, 0, v132
	s_waitcnt vmcnt(0)
	v_rcp_f32_e32 v7, v128
	s_getpc_b64 s[36:37]
	s_sub_u32 s36, s36, 0x9790
	s_subb_u32 s37, s37, 0
	v_lshlrev_b32_e32 v183, 6, v0
	v_min_u32_e32 v183, 0x1d80, v183
	global_load_dword v183, v183, s[36:37]
	v_lshlrev_b32_e32 v182, 6, v38
	global_load_dword v182, v182, s[38:39]
	s_lshl_b32 s40, s29, 10
	s_add_u32 s40, s42, s40
	s_addc_u32 s41, s43, 0
	v_lshlrev_b32_e32 v181, 6, v0
	v_and_b32_e32 v181, 0x7fc0, v181
	global_load_dword v181, v181, s[40:41]
	s_mov_b32 s4, 0x42c80000
	v_cndmask_b32_e32 v3, 0, v3, vcc
	v_cmp_lt_f32_e32 vcc, 0, v131
	v_cmp_ngt_f32_e64 s[2:3], s4, v3
	s_mov_b64 s[6:7], 0
	v_cndmask_b32_e32 v4, 0, v4, vcc
	v_cmp_lt_f32_e32 vcc, 0, v130
	s_nop 1
	v_cndmask_b32_e32 v5, 0, v5, vcc
	v_cmp_lt_f32_e32 vcc, 0, v129
	s_nop 1
	v_cndmask_b32_e32 v6, 0, v6, vcc
	v_cmp_lt_f32_e32 vcc, 0, v128
	s_nop 1
	v_cndmask_b32_e32 v7, 0, v7, vcc
	v_cmp_ngt_f32_e32 vcc, s4, v2
	s_or_b64 s[2:3], vcc, s[2:3]
	v_cmp_ngt_f32_e32 vcc, s4, v4
	s_or_b64 s[2:3], s[2:3], vcc
	v_cmp_ngt_f32_e32 vcc, s4, v5
	s_or_b64 s[2:3], s[2:3], vcc
	v_cmp_ngt_f32_e32 vcc, s4, v6
	s_or_b64 s[2:3], s[2:3], vcc
	v_cmp_ngt_f32_e32 vcc, s4, v7
	s_or_b64 s[2:3], s[2:3], vcc
	v_cndmask_b32_e64 v8, 0, 1, s[2:3]
	v_cmp_ne_u32_e32 vcc, 0, v8
	s_cmp_eq_u64 vcc, 0
	s_cselect_b64 s[2:3], -1, 0
	v_cndmask_b32_e64 v8, 0, 1, s[2:3]
	s_nop 0
	v_readfirstlane_b32 s2, v8
	s_bitcmp0_b32 s2, 0
	s_cbranch_scc0 .LBB4_45
	s_cmp_lt_i32 s28, 4
	s_cbranch_scc1 .LBB4_46
	s_cmp_gt_i32 s28, 4
	s_cbranch_scc0 .LBB4_47
	s_mov_b64 s[4:5], -1
	v_mov_b32_e32 v8, 0
	s_cmp_gt_i32 s28, 5
	v_mov_b32_e32 v167, 0
	v_mov_b32_e32 v166, 0
	v_mov_b32_e32 v165, 0
	v_mov_b32_e32 v164, 0
	v_mov_b32_e32 v162, 0
	v_mov_b32_e32 v160, 0
	v_mov_b32_e32 v159, 0
	v_mov_b32_e32 v157, 0
	v_mov_b32_e32 v151, 0
	v_mov_b32_e32 v149, 0
	v_mov_b32_e32 v147, 0
	v_mov_b32_e32 v146, 0
	v_mov_b32_e32 v144, 0
	v_mov_b32_e32 v143, 0
	v_mov_b32_e32 v152, 0
	v_mov_b32_e32 v153, 0
	v_mov_b32_e32 v154, 0
	v_mov_b32_e32 v155, 0
	v_mov_b32_e32 v156, 0
	v_mov_b32_e32 v158, 0
	v_mov_b32_e32 v161, 0
	v_mov_b32_e32 v163, 0
	v_mov_b32_e32 v168, 0
	v_mov_b32_e32 v169, 0
	v_mov_b32_e32 v170, 0
	v_mov_b32_e32 v171, 0
	v_mov_b32_e32 v172, 0
	v_mov_b32_e32 v173, 0
	v_mov_b32_e32 v174, 0
	v_mov_b32_e32 v145, 0
	v_mov_b32_e32 v148, 0
	v_mov_b32_e32 v150, 0
	s_cbranch_scc0 .LBB4_50
	s_cmp_eq_u32 s28, 6
	s_cbranch_scc0 .LBB4_49
	v_mov_b32_e32 v145, 0
	v_mov_b32_e32 v148, 0
	v_mov_b32_e32 v150, 0
	v_mov_b32_e32 v143, 0
	v_mov_b32_e32 v144, 0
	v_mov_b32_e32 v146, 0
	v_mov_b32_e32 v147, 0
	v_mov_b32_e32 v149, 0
	v_mov_b32_e32 v151, 0
	v_mov_b32_e32 v152, 0
	v_mov_b32_e32 v153, 0
	v_mov_b32_e32 v154, 0
	v_mov_b32_e32 v155, 0
	v_mov_b32_e32 v156, 0
	v_mov_b32_e32 v158, 0
	v_mov_b32_e32 v161, 0
	v_mov_b32_e32 v163, 0
	v_mov_b32_e32 v157, 0
	v_mov_b32_e32 v159, 0
	v_mov_b32_e32 v160, 0
	v_mov_b32_e32 v162, 0
	v_mov_b32_e32 v164, 0
	v_mov_b32_e32 v165, 0
	v_mov_b32_e32 v166, 0
	v_mov_b32_e32 v167, 0
	v_mov_b32_e32 v168, 0
	v_mov_b32_e32 v169, 0
	v_mov_b32_e32 v170, 0
	v_mov_b32_e32 v171, 0
	v_mov_b32_e32 v172, 0
	v_mov_b32_e32 v173, 0
	v_mov_b32_e32 v174, 0
	v_fma_mix_f32 v148, v43, v7, v148 op_sel_hi:[1,0,0]
	v_fma_mix_f32 v150, v45, v7, v150 op_sel_hi:[1,0,0]
	v_fma_mix_f32 v143, v50, v7, v143 op_sel_hi:[1,0,0]
	v_fma_mix_f32 v144, v54, v7, v144 op_sel_hi:[1,0,0]
	v_fma_mix_f32 v146, v58, v7, v146 op_sel_hi:[1,0,0]
	v_fma_mix_f32 v147, v61, v7, v147 op_sel_hi:[1,0,0]
	v_fma_mix_f32 v149, v64, v7, v149 op_sel_hi:[1,0,0]
	v_fma_mix_f32 v151, v66, v7, v151 op_sel_hi:[1,0,0]
	v_fma_mix_f32 v152, v43, v7, v152 op_sel:[1,0,0] op_sel_hi:[1,0,0]
	v_fma_mix_f32 v153, v45, v7, v153 op_sel:[1,0,0] op_sel_hi:[1,0,0]
	v_fma_mix_f32 v154, v50, v7, v154 op_sel:[1,0,0] op_sel_hi:[1,0,0]
	v_fma_mix_f32 v155, v54, v7, v155 op_sel:[1,0,0] op_sel_hi:[1,0,0]
	v_fma_mix_f32 v156, v58, v7, v156 op_sel:[1,0,0] op_sel_hi:[1,0,0]
	v_fma_mix_f32 v158, v61, v7, v158 op_sel:[1,0,0] op_sel_hi:[1,0,0]
	v_fma_mix_f32 v161, v64, v7, v161 op_sel:[1,0,0] op_sel_hi:[1,0,0]
	v_fma_mix_f32 v163, v66, v7, v163 op_sel:[1,0,0] op_sel_hi:[1,0,0]
	v_fma_mix_f32 v157, v72, v7, v157 op_sel_hi:[1,0,0]
	v_fma_mix_f32 v159, v76, v7, v159 op_sel_hi:[1,0,0]
	v_fma_mix_f32 v160, v83, v7, v160 op_sel_hi:[1,0,0]
	v_fma_mix_f32 v162, v85, v7, v162 op_sel_hi:[1,0,0]
	v_fma_mix_f32 v164, v89, v7, v164 op_sel_hi:[1,0,0]
	v_fma_mix_f32 v165, v92, v7, v165 op_sel_hi:[1,0,0]
	v_fma_mix_f32 v166, v95, v7, v166 op_sel_hi:[1,0,0]
	v_fma_mix_f32 v167, v96, v7, v167 op_sel_hi:[1,0,0]
	v_fma_mix_f32 v168, v72, v7, v168 op_sel:[1,0,0] op_sel_hi:[1,0,0]
	v_fma_mix_f32 v169, v76, v7, v169 op_sel:[1,0,0] op_sel_hi:[1,0,0]
	v_fma_mix_f32 v170, v83, v7, v170 op_sel:[1,0,0] op_sel_hi:[1,0,0]
	v_fma_mix_f32 v171, v85, v7, v171 op_sel:[1,0,0] op_sel_hi:[1,0,0]
	v_fma_mix_f32 v172, v89, v7, v172 op_sel:[1,0,0] op_sel_hi:[1,0,0]
	v_fma_mix_f32 v173, v92, v7, v173 op_sel:[1,0,0] op_sel_hi:[1,0,0]
	v_fma_mix_f32 v174, v95, v7, v174 op_sel:[1,0,0] op_sel_hi:[1,0,0]
	v_fma_mix_f32 v145, v96, v7, v145 op_sel:[1,0,0] op_sel_hi:[1,0,0]
	s_branch .LBB4_50

	.amdhsa_kernel _Z6k_iterILb0ELb1EEvPKfS1_PKiPK15HIP_vector_typeIfLj4EES7_S1_S1_S3_S1_PfS8_S1_S3_PDF16_PS5_SA_PiSA_SB_
		.amdhsa_group_segment_fixed_size 5808
		.amdhsa_private_segment_fixed_size 0
		.amdhsa_kernarg_size 152
		.amdhsa_user_sgpr_count 2
		.amdhsa_user_sgpr_dispatch_ptr 0
		.amdhsa_user_sgpr_queue_ptr 0
		.amdhsa_user_sgpr_kernarg_segment_ptr 1
		.amdhsa_user_sgpr_dispatch_id 0
		.amdhsa_user_sgpr_kernarg_preload_length 0
		.amdhsa_user_sgpr_kernarg_preload_offset 0
		.amdhsa_user_sgpr_private_segment_size 0
		.amdhsa_uses_dynamic_stack 0
		.amdhsa_enable_private_segment 0
		.amdhsa_system_sgpr_workgroup_id_x 1
		.amdhsa_system_sgpr_workgroup_id_y 0
		.amdhsa_system_sgpr_workgroup_id_z 0
		.amdhsa_system_sgpr_workgroup_info 0
		.amdhsa_system_vgpr_workitem_id 0
		.amdhsa_next_free_vgpr 216
		.amdhsa_next_free_sgpr 48
		.amdhsa_accum_offset 216
		.amdhsa_reserve_vcc 1
		.amdhsa_float_round_mode_32 0
		.amdhsa_float_round_mode_16_64 0
		.amdhsa_float_denorm_mode_32 3
		.amdhsa_float_denorm_mode_16_64 3
		.amdhsa_dx10_clamp 1
		.amdhsa_ieee_mode 1
		.amdhsa_fp16_overflow 0
		.amdhsa_tg_split 0
		.amdhsa_exception_fp_ieee_invalid_op 0
		.amdhsa_exception_fp_denorm_src 0
		.amdhsa_exception_fp_ieee_div_zero 0
		.amdhsa_exception_fp_ieee_overflow 0
		.amdhsa_exception_fp_ieee_underflow 0
		.amdhsa_exception_fp_ieee_inexact 0
		.amdhsa_exception_int_div_zero 0
	.end_amdhsa_kernel

amdhsa.kernels:
  - .agpr_count:     0
    .args:
      - .actual_access:  read_only
        .address_space:  global
        .offset:         0
        .size:           8
        .value_kind:     global_buffer
      - .actual_access:  read_only
        .address_space:  global
        .offset:         8
        .size:           8
        .value_kind:     global_buffer
      - .actual_access:  read_only
        .address_space:  global
        .offset:         16
        .size:           8
        .value_kind:     global_buffer
      - .actual_access:  read_only
        .address_space:  global
        .offset:         24
        .size:           8
        .value_kind:     global_buffer
      - .actual_access:  write_only
        .address_space:  global
        .offset:         32
        .size:           8
        .value_kind:     global_buffer
      - .actual_access:  write_only
        .address_space:  global
        .offset:         40
        .size:           8
        .value_kind:     global_buffer
      - .actual_access:  write_only
        .address_space:  global
        .offset:         48
        .size:           8
        .value_kind:     global_buffer
      - .actual_access:  write_only
        .address_space:  global
        .offset:         56
        .size:           8
        .value_kind:     global_buffer
      - .actual_access:  write_only
        .address_space:  global
        .offset:         64
        .size:           8
        .value_kind:     global_buffer
      - .actual_access:  write_only
        .address_space:  global
        .offset:         72
        .size:           8
        .value_kind:     global_buffer
      - .actual_access:  write_only
        .address_space:  global
        .offset:         80
        .size:           8
        .value_kind:     global_buffer
      - .actual_access:  write_only
        .address_space:  global
        .offset:         88
        .size:           8
        .value_kind:     global_buffer
      - .actual_access:  write_only
        .address_space:  global
        .offset:         96
        .size:           8
        .value_kind:     global_buffer
      - .actual_access:  write_only
        .address_space:  global
        .offset:         104
        .size:           8
        .value_kind:     global_buffer
      - .actual_access:  write_only
        .address_space:  global
        .offset:         112
        .size:           8
        .value_kind:     global_buffer
    .group_segment_fixed_size: 67584
    .kernarg_segment_align: 8
    .kernarg_segment_size: 120
    .language:       OpenCL C
    .language_version:
      - 2
      - 0
    .max_flat_workgroup_size: 1024
    .name:           _Z6k_sortPKfS0_PKiS2_PiP15HIP_vector_typeIfLj4EEPfS7_S3_S7_S7_S3_S3_S6_S6_
    .private_segment_fixed_size: 0
    .sgpr_count:     58
    .sgpr_spill_count: 0
    .symbol:         _Z6k_sortPKfS0_PKiS2_PiP15HIP_vector_typeIfLj4EEPfS7_S3_S7_S7_S3_S3_S6_S6_.kd
    .uniform_work_group_size: 1
    .uses_dynamic_stack: false
    .vgpr_count:     48
    .vgpr_spill_count: 0
    .wavefront_size: 64
  - .agpr_count:     0
    .args:
      - .actual_access:  read_only
        .address_space:  global
        .offset:         0
        .size:           8
        .value_kind:     global_buffer
      - .actual_access:  read_only
        .address_space:  global
        .offset:         8
        .size:           8
        .value_kind:     global_buffer
      - .actual_access:  read_only
        .address_space:  global
        .offset:         16
        .size:           8
        .value_kind:     global_buffer
      - .actual_access:  read_only
        .address_space:  global
        .offset:         24
        .size:           8
        .value_kind:     global_buffer
      - .actual_access:  read_only
        .address_space:  global
        .offset:         32
        .size:           8
        .value_kind:     global_buffer
      - .actual_access:  read_only
        .address_space:  global
        .offset:         40
        .size:           8
        .value_kind:     global_buffer
      - .actual_access:  read_only
        .address_space:  global
        .offset:         48
        .size:           8
        .value_kind:     global_buffer
      - .actual_access:  write_only
        .address_space:  global
        .offset:         56
        .size:           8
        .value_kind:     global_buffer
    .group_segment_fixed_size: 145952
    .kernarg_segment_align: 8
    .kernarg_segment_size: 64
    .language:       OpenCL C
    .language_version:
      - 2
      - 0
    .max_flat_workgroup_size: 512
    .name:           _Z7k_finalPK15HIP_vector_typeIfLj4EES2_PKiS4_PKfS6_PKDF16_Pf
    .private_segment_fixed_size: 0
    .sgpr_count:     34
    .sgpr_spill_count: 0
    .symbol:         _Z7k_finalPK15HIP_vector_typeIfLj4EES2_PKiS4_PKfS6_PKDF16_Pf.kd
    .uniform_work_group_size: 1
    .uses_dynamic_stack: false
    .vgpr_count:     177
    .vgpr_spill_count: 0
    .wavefront_size: 64
  - .agpr_count:     0
    .args:
      - .actual_access:  read_only
        .address_space:  global
        .offset:         0
        .size:           8
        .value_kind:     global_buffer
      - .actual_access:  read_only
        .address_space:  global
        .offset:         8
        .size:           8
        .value_kind:     global_buffer
      - .actual_access:  read_only
        .address_space:  global
        .offset:         16
        .size:           8
        .value_kind:     global_buffer
      - .actual_access:  read_only
        .address_space:  global
        .offset:         24
        .size:           8
        .value_kind:     global_buffer
      - .actual_access:  read_only
        .address_space:  global
        .offset:         32
        .size:           8
        .value_kind:     global_buffer
      - .actual_access:  read_only
        .address_space:  global
        .offset:         40
        .size:           8
        .value_kind:     global_buffer
      - .actual_access:  read_only
        .address_space:  global
        .offset:         48
        .size:           8
        .value_kind:     global_buffer
      - .actual_access:  read_only
        .address_space:  global
        .offset:         56
        .size:           8
        .value_kind:     global_buffer
      - .actual_access:  read_only
        .address_space:  global
        .offset:         64
        .size:           8
        .value_kind:     global_buffer
      - .address_space:  global
        .offset:         72
        .size:           8
        .value_kind:     global_buffer
      - .actual_access:  read_only
        .address_space:  global
        .offset:         80
        .size:           8
        .value_kind:     global_buffer
      - .actual_access:  read_only
        .address_space:  global
        .offset:         88
        .size:           8
        .value_kind:     global_buffer
      - .actual_access:  read_only
        .address_space:  global
        .offset:         96
        .size:           8
        .value_kind:     global_buffer
      - .actual_access:  write_only
        .address_space:  global
        .offset:         104
        .size:           8
        .value_kind:     global_buffer
      - .address_space:  global
        .offset:         112
        .size:           8
        .value_kind:     global_buffer
      - .actual_access:  write_only
        .address_space:  global
        .offset:         120
        .size:           8
        .value_kind:     global_buffer
      - .actual_access:  write_only
        .address_space:  global
        .offset:         128
        .size:           8
        .value_kind:     global_buffer
      - .actual_access:  write_only
        .address_space:  global
        .offset:         136
        .size:           8
        .value_kind:     global_buffer
      - .actual_access:  write_only
        .address_space:  global
        .offset:         144
        .size:           8
        .value_kind:     global_buffer
    .group_segment_fixed_size: 30384
    .kernarg_segment_align: 8
    .kernarg_segment_size: 152
    .language:       OpenCL C
    .language_version:
      - 2
      - 0
    .max_flat_workgroup_size: 512
    .name:           _Z6k_iterILb1ELb0EEvPKfS1_PKiPK15HIP_vector_typeIfLj4EES7_S1_S1_S3_S1_PfS8_S1_S3_PDF16_PS5_SA_PiSA_SB_
    .private_segment_fixed_size: 0
    .sgpr_count:     108
    .sgpr_spill_count: 0
    .symbol:         _Z6k_iterILb1ELb0EEvPKfS1_PKiPK15HIP_vector_typeIfLj4EES7_S1_S1_S3_S1_PfS8_S1_S3_PDF16_PS5_SA_PiSA_SB_.kd
    .uniform_work_group_size: 1
    .uses_dynamic_stack: false
    .vgpr_count:     256
    .vgpr_spill_count: 0
    .wavefront_size: 64
  - .agpr_count:     0
    .args:
      - .actual_access:  read_only
        .address_space:  global
        .offset:         0
        .size:           8
        .value_kind:     global_buffer
      - .actual_access:  read_only
        .address_space:  global
        .offset:         8
        .size:           8
        .value_kind:     global_buffer
      - .actual_access:  read_only
        .address_space:  global
        .offset:         16
        .size:           8
        .value_kind:     global_buffer
      - .actual_access:  read_only
        .address_space:  global
        .offset:         24
        .size:           8
        .value_kind:     global_buffer
      - .actual_access:  read_only
        .address_space:  global
        .offset:         32
        .size:           8
        .value_kind:     global_buffer
      - .actual_access:  read_only
        .address_space:  global
        .offset:         40
        .size:           8
        .value_kind:     global_buffer
      - .actual_access:  read_only
        .address_space:  global
        .offset:         48
        .size:           8
        .value_kind:     global_buffer
      - .actual_access:  read_only
        .address_space:  global
        .offset:         56
        .size:           8
        .value_kind:     global_buffer
      - .actual_access:  read_only
        .address_space:  global
        .offset:         64
        .size:           8
        .value_kind:     global_buffer
      - .address_space:  global
        .offset:         72
        .size:           8
        .value_kind:     global_buffer
      - .actual_access:  read_only
        .address_space:  global
        .offset:         80
        .size:           8
        .value_kind:     global_buffer
      - .actual_access:  read_only
        .address_space:  global
        .offset:         88
        .size:           8
        .value_kind:     global_buffer
      - .actual_access:  read_only
        .address_space:  global
        .offset:         96
        .size:           8
        .value_kind:     global_buffer
      - .actual_access:  read_only
        .address_space:  global
        .offset:         104
        .size:           8
        .value_kind:     global_buffer
      - .actual_access:  read_only
        .address_space:  global
        .offset:         112
        .size:           8
        .value_kind:     global_buffer
      - .actual_access:  read_only
        .address_space:  global
        .offset:         120
        .size:           8
        .value_kind:     global_buffer
      - .actual_access:  read_only
        .address_space:  global
        .offset:         128
        .size:           8
        .value_kind:     global_buffer
      - .actual_access:  read_only
        .address_space:  global
        .offset:         136
        .size:           8
        .value_kind:     global_buffer
      - .actual_access:  read_only
        .address_space:  global
        .offset:         144
        .size:           8
        .value_kind:     global_buffer
    .group_segment_fixed_size: 5808
    .kernarg_segment_align: 8
    .kernarg_segment_size: 152
    .language:       OpenCL C
    .language_version:
      - 2
      - 0
    .max_flat_workgroup_size: 512
    .name:           _Z6k_iterILb0ELb0EEvPKfS1_PKiPK15HIP_vector_typeIfLj4EES7_S1_S1_S3_S1_PfS8_S1_S3_PDF16_PS5_SA_PiSA_SB_
    .private_segment_fixed_size: 0
    .sgpr_count:     54
    .sgpr_spill_count: 0
    .symbol:         _Z6k_iterILb0ELb0EEvPKfS1_PKiPK15HIP_vector_typeIfLj4EES7_S1_S1_S3_S1_PfS8_S1_S3_PDF16_PS5_SA_PiSA_SB_.kd
    .uniform_work_group_size: 1
    .uses_dynamic_stack: false
    .vgpr_count:     216
    .vgpr_spill_count: 0
    .wavefront_size: 64
  - .agpr_count:     0
    .args:
      - .actual_access:  read_only
        .address_space:  global
        .offset:         0
        .size:           8
        .value_kind:     global_buffer
      - .actual_access:  read_only
        .address_space:  global
        .offset:         8
        .size:           8
        .value_kind:     global_buffer
      - .actual_access:  read_only
        .address_space:  global
        .offset:         16
        .size:           8
        .value_kind:     global_buffer
      - .actual_access:  read_only
        .address_space:  global
        .offset:         24
        .size:           8
        .value_kind:     global_buffer
      - .actual_access:  read_only
        .address_space:  global
        .offset:         32
        .size:           8
        .value_kind:     global_buffer
      - .actual_access:  read_only
        .address_space:  global
        .offset:         40
        .size:           8
        .value_kind:     global_buffer
      - .actual_access:  read_only
        .address_space:  global
        .offset:         48
        .size:           8
        .value_kind:     global_buffer
      - .actual_access:  read_only
        .address_space:  global
        .offset:         56
        .size:           8
        .value_kind:     global_buffer
      - .actual_access:  read_only
        .address_space:  global
        .offset:         64
        .size:           8
        .value_kind:     global_buffer
      - .address_space:  global
        .offset:         72
        .size:           8
        .value_kind:     global_buffer
      - .actual_access:  write_only
        .address_space:  global
        .offset:         80
        .size:           8
        .value_kind:     global_buffer
      - .actual_access:  read_only
        .address_space:  global
        .offset:         88
        .size:           8
        .value_kind:     global_buffer
      - .actual_access:  read_only
        .address_space:  global
        .offset:         96
        .size:           8
        .value_kind:     global_buffer
      - .actual_access:  read_only
        .address_space:  global
        .offset:         104
        .size:           8
        .value_kind:     global_buffer
      - .actual_access:  read_only
        .address_space:  global
        .offset:         112
        .size:           8
        .value_kind:     global_buffer
      - .actual_access:  read_only
        .address_space:  global
        .offset:         120
        .size:           8
        .value_kind:     global_buffer
      - .actual_access:  read_only
        .address_space:  global
        .offset:         128
        .size:           8
        .value_kind:     global_buffer
      - .actual_access:  read_only
        .address_space:  global
        .offset:         136
        .size:           8
        .value_kind:     global_buffer
      - .actual_access:  read_only
        .address_space:  global
        .offset:         144
        .size:           8
        .value_kind:     global_buffer
    .group_segment_fixed_size: 5808
    .kernarg_segment_align: 8
    .kernarg_segment_size: 152
    .language:       OpenCL C
    .language_version:
      - 2
      - 0
    .max_flat_workgroup_size: 512
    .name:           _Z6k_iterILb0ELb1EEvPKfS1_PKiPK15HIP_vector_typeIfLj4EES7_S1_S1_S3_S1_PfS8_S1_S3_PDF16_PS5_SA_PiSA_SB_
    .private_segment_fixed_size: 0
    .sgpr_count:     54
    .sgpr_spill_count: 0
    .symbol:         _Z6k_iterILb0ELb1EEvPKfS1_PKiPK15HIP_vector_typeIfLj4EES7_S1_S1_S3_S1_PfS8_S1_S3_PDF16_PS5_SA_PiSA_SB_.kd
    .uniform_work_group_size: 1
    .uses_dynamic_stack: false
    .vgpr_count:     216
    .vgpr_spill_count: 0
    .wavefront_size: 64
